# LayerNorm epilogues: 122 broadcast v_pk_mul_f32 (scalar x pair) split into scalar v_mul_f32 pairs, same code size
# speedup vs baseline: 1.0039x; 1.0039x over previous
.LBB0_578:
	v_and_b32_e32 v183, 63, v126
	v_bfe_u32 v184, v126, 4, 2
	s_lshl_b32 s5, s9, 5
	s_lshl_b32 s4, s11, 8
	s_barrier
	s_or_b32 s5, s4, s5
	v_add_u32_e32 v182, s40, v0
	v_lshl_add_u32 v162, v184, 3, s5
	v_lshl_add_u32 v178, s0, 8, v182
	v_ashrrev_i32_e32 v163, 31, v162
	v_ashrrev_i32_e32 v179, 31, v178
	v_lshl_add_u64 v[180:181], v[162:163], 2, s[22:23]
	v_lshlrev_b64 v[126:127], 13, v[178:179]
	v_add_u32_e32 v174, 16, v178
	s_mov_b32 s6, 0.5
	s_mov_b32 s24, 0x3fd744fd
	s_mov_b32 s5, s26
	v_lshl_add_u64 v[134:135], v[180:181], 0, v[126:127]
	v_ashrrev_i32_e32 v175, 31, v174
	global_load_dwordx4 v[126:129], v[134:135], off offset:16
	global_load_dwordx4 v[154:157], v[134:135], off
	global_load_dwordx4 v[158:161], v[134:135], off offset:528
	global_load_dwordx4 v[164:167], v[134:135], off offset:512
	v_lshlrev_b64 v[134:135], 13, v[174:175]
	v_lshl_add_u64 v[134:135], v[180:181], 0, v[134:135]
	global_load_dwordx4 v[186:189], v[134:135], off offset:16
	global_load_dwordx4 v[190:193], v[134:135], off
	global_load_dwordx4 v[194:197], v[134:135], off offset:528
	global_load_dwordx4 v[198:201], v[134:135], off offset:512
	v_add_u32_e32 v172, 32, v178
	v_ashrrev_i32_e32 v173, 31, v172
	v_lshlrev_b64 v[134:135], 13, v[172:173]
	v_lshl_add_u64 v[134:135], v[180:181], 0, v[134:135]
	global_load_dwordx4 v[204:207], v[134:135], off offset:16
	global_load_dwordx4 v[208:211], v[134:135], off
	global_load_dwordx4 v[150:153], v[134:135], off offset:528
	global_load_dwordx4 v[212:215], v[134:135], off offset:512
	v_add_u32_e32 v170, 48, v178
	v_ashrrev_i32_e32 v171, 31, v170
	v_lshlrev_b64 v[134:135], 13, v[170:171]
	v_lshl_add_u64 v[142:143], v[180:181], 0, v[134:135]
	global_load_dwordx4 v[138:141], v[142:143], off offset:16
	global_load_dwordx4 v[146:149], v[142:143], off
	global_load_dwordx4 v[134:137], v[142:143], off offset:528
	s_nop 0
	global_load_dwordx4 v[142:145], v[142:143], off offset:512
	v_pk_mul_f32 v[118:119], v[118:119], s[6:7] op_sel_hi:[1,0]
	v_pk_mul_f32 v[120:121], v[120:121], s[6:7] op_sel_hi:[1,0]
	v_pk_mul_f32 v[122:123], v[122:123], s[6:7] op_sel_hi:[1,0]
	v_add_u32_e32 v176, 0x80, v178
	v_pk_mul_f32 v[124:125], v[124:125], s[6:7] op_sel_hi:[1,0]
	v_pk_mul_f32 v[30:31], v[30:31], s[6:7] op_sel_hi:[1,0]
	v_pk_mul_f32 v[32:33], v[32:33], s[6:7] op_sel_hi:[1,0]
	v_ashrrev_i32_e32 v177, 31, v176
	v_add_u32_e32 v168, 0x90, v178
	v_ashrrev_i32_e32 v169, 31, v168
	s_lshl_b32 s5, s9, 3
	v_cmp_eq_u32_e32 vcc, 0, v184
	s_add_i32 s5, s5, 0
	s_waitcnt vmcnt(15)
	v_pk_fma_f32 v[126:127], v[126:127], s[24:25], v[118:119] op_sel_hi:[1,0,1]
	v_pk_fma_f32 v[128:129], v[128:129], s[24:25], v[120:121] op_sel_hi:[1,0,1]
	s_waitcnt vmcnt(13)
	v_mul_f32_e32 v118, s24, v160
	v_mul_f32_e32 v119, s24, v161
	v_mul_f32_e32 v120, s24, v158
	v_mul_f32_e32 v121, s24, v159
	v_pk_fma_f32 v[36:37], v[36:37], s[6:7], v[118:119] op_sel_hi:[1,0,1]
	s_waitcnt vmcnt(10)
	v_mul_f32_e32 v118, s24, v192
	v_mul_f32_e32 v119, s24, v193
	v_pk_fma_f32 v[122:123], v[154:155], s[24:25], v[122:123] op_sel_hi:[1,0,1]
	v_pk_fma_f32 v[34:35], v[34:35], s[6:7], v[120:121] op_sel_hi:[1,0,1]
	v_mul_f32_e32 v120, s24, v190
	v_mul_f32_e32 v121, s24, v191
	v_pk_fma_f32 v[116:117], v[116:117], s[6:7], v[118:119] op_sel_hi:[1,0,1]
	v_mul_f32_e32 v118, s24, v188
	v_mul_f32_e32 v119, s24, v189
	v_mul_f32_e32 v154, s24, v186
	v_mul_f32_e32 v155, s24, v187
	v_pk_fma_f32 v[114:115], v[114:115], s[6:7], v[120:121] op_sel_hi:[1,0,1]
	v_pk_fma_f32 v[120:121], v[112:113], s[6:7], v[118:119] op_sel_hi:[1,0,1]
	v_pk_fma_f32 v[118:119], v[110:111], s[6:7], v[154:155] op_sel_hi:[1,0,1]
	s_waitcnt vmcnt(8)
	v_mul_f32_e32 v110, s24, v200
	v_mul_f32_e32 v111, s24, v201
	v_mul_f32_e32 v112, s24, v198
	v_mul_f32_e32 v113, s24, v199
	v_pk_fma_f32 v[12:13], v[12:13], s[6:7], v[110:111] op_sel_hi:[1,0,1]
	v_mul_f32_e32 v110, s24, v196
	v_mul_f32_e32 v111, s24, v197
	v_pk_fma_f32 v[10:11], v[10:11], s[6:7], v[112:113] op_sel_hi:[1,0,1]
	v_mul_f32_e32 v112, s24, v194
	v_mul_f32_e32 v113, s24, v195
	v_pk_fma_f32 v[16:17], v[16:17], s[6:7], v[110:111] op_sel_hi:[1,0,1]
	s_waitcnt vmcnt(6)
	v_mul_f32_e32 v110, s24, v210
	v_mul_f32_e32 v111, s24, v211
	v_pk_fma_f32 v[14:15], v[14:15], s[6:7], v[112:113] op_sel_hi:[1,0,1]
	v_mul_f32_e32 v112, s24, v208
	v_mul_f32_e32 v113, s24, v209
	v_pk_fma_f32 v[100:101], v[100:101], s[6:7], v[110:111] op_sel_hi:[1,0,1]
	v_mul_f32_e32 v110, s24, v206
	v_mul_f32_e32 v111, s24, v207
	v_mul_f32_e32 v154, s24, v204
	v_mul_f32_e32 v155, s24, v205
	v_pk_fma_f32 v[98:99], v[98:99], s[6:7], v[112:113] op_sel_hi:[1,0,1]
	v_pk_fma_f32 v[112:113], v[108:109], s[6:7], v[110:111] op_sel_hi:[1,0,1]
	v_pk_fma_f32 v[110:111], v[106:107], s[6:7], v[154:155] op_sel_hi:[1,0,1]
	s_waitcnt vmcnt(4)
	v_mul_f32_e32 v106, s24, v214
	v_mul_f32_e32 v107, s24, v215
	v_mul_f32_e32 v108, s24, v212
	v_mul_f32_e32 v109, s24, v213
	v_pk_fma_f32 v[20:21], v[20:21], s[6:7], v[106:107] op_sel_hi:[1,0,1]
	v_mul_f32_e32 v106, s24, v152
	v_mul_f32_e32 v107, s24, v153
	v_pk_fma_f32 v[18:19], v[18:19], s[6:7], v[108:109] op_sel_hi:[1,0,1]
	v_mul_f32_e32 v108, s24, v150
	v_mul_f32_e32 v109, s24, v151
	v_pk_fma_f32 v[24:25], v[24:25], s[6:7], v[106:107] op_sel_hi:[1,0,1]
	s_waitcnt vmcnt(2)
	v_mul_f32_e32 v106, s24, v148
	v_mul_f32_e32 v107, s24, v149
	v_pk_fma_f32 v[22:23], v[22:23], s[6:7], v[108:109] op_sel_hi:[1,0,1]
	v_mul_f32_e32 v108, s24, v146
	v_mul_f32_e32 v109, s24, v147
	v_pk_fma_f32 v[104:105], v[104:105], s[6:7], v[106:107] op_sel_hi:[1,0,1]
	v_mul_f32_e32 v106, s24, v140
	v_mul_f32_e32 v107, s24, v141
	v_mul_f32_e32 v138, s24, v138
	v_mul_f32_e32 v139, s24, v139
	v_pk_fma_f32 v[102:103], v[102:103], s[6:7], v[108:109] op_sel_hi:[1,0,1]
	v_pk_fma_f32 v[108:109], v[4:5], s[6:7], v[106:107] op_sel_hi:[1,0,1]
	v_pk_fma_f32 v[106:107], v[2:3], s[6:7], v[138:139] op_sel_hi:[1,0,1]
	s_waitcnt vmcnt(0)
	v_mul_f32_e32 v2, s24, v144
	v_mul_f32_e32 v3, s24, v145
	v_mul_f32_e32 v138, s24, v142
	v_mul_f32_e32 v139, s24, v143
	v_pk_fma_f32 v[4:5], v[96:97], s[6:7], v[2:3] op_sel_hi:[1,0,1]
	v_pk_fma_f32 v[2:3], v[94:95], s[6:7], v[138:139] op_sel_hi:[1,0,1]
	v_mul_f32_e32 v94, s24, v136
	v_mul_f32_e32 v95, s24, v137
	v_mul_f32_e32 v96, s24, v134
	v_mul_f32_e32 v97, s24, v135
	v_pk_fma_f32 v[124:125], v[156:157], s[24:25], v[124:125] op_sel_hi:[1,0,1]
	v_pk_fma_f32 v[32:33], s[24:25], v[166:167], v[32:33] op_sel_hi:[0,1,1]
	v_pk_fma_f32 v[30:31], s[24:25], v[164:165], v[30:31] op_sel_hi:[0,1,1]
	v_pk_fma_f32 v[8:9], v[8:9], s[6:7], v[94:95] op_sel_hi:[1,0,1]
	v_pk_fma_f32 v[6:7], v[6:7], s[6:7], v[96:97] op_sel_hi:[1,0,1]
	v_lshlrev_b64 v[94:95], 13, v[176:177]
	v_lshl_add_u64 v[94:95], v[180:181], 0, v[94:95]
	global_load_dwordx4 v[186:189], v[94:95], off offset:16
	global_load_dwordx4 v[190:193], v[94:95], off
	global_load_dwordx4 v[194:197], v[94:95], off offset:528
	global_load_dwordx4 v[198:201], v[94:95], off offset:512
	v_lshlrev_b64 v[94:95], 13, v[168:169]
	v_add_u32_e32 v166, 0xa0, v178
	v_lshl_add_u64 v[94:95], v[180:181], 0, v[94:95]
	v_ashrrev_i32_e32 v167, 31, v166
	global_load_dwordx4 v[204:207], v[94:95], off offset:16
	global_load_dwordx4 v[208:211], v[94:95], off
	global_load_dwordx4 v[212:215], v[94:95], off offset:528
	global_load_dwordx4 v[216:219], v[94:95], off offset:512
	v_lshlrev_b64 v[94:95], 13, v[166:167]
	v_lshl_add_u64 v[134:135], v[180:181], 0, v[94:95]
	global_load_dwordx4 v[94:97], v[134:135], off offset:16
	global_load_dwordx4 v[158:161], v[134:135], off
	global_load_dwordx4 v[150:153], v[134:135], off offset:528
	global_load_dwordx4 v[154:157], v[134:135], off offset:512
	v_add_u32_e32 v164, 0xb0, v178
	v_ashrrev_i32_e32 v165, 31, v164
	v_lshlrev_b64 v[134:135], 13, v[164:165]
	v_lshl_add_u64 v[142:143], v[180:181], 0, v[134:135]
	global_load_dwordx4 v[138:141], v[142:143], off offset:16
	global_load_dwordx4 v[146:149], v[142:143], off
	global_load_dwordx4 v[134:137], v[142:143], off offset:528
	s_nop 0
	global_load_dwordx4 v[142:145], v[142:143], off offset:512
	s_waitcnt vmcnt(15)
	v_mul_f32_e32 v186, s24, v186
	v_mul_f32_e32 v187, s24, v187
	s_waitcnt vmcnt(14)
	v_mul_f32_e32 v180, s24, v192
	v_mul_f32_e32 v181, s24, v193
	v_pk_fma_f32 v[76:77], v[76:77], s[6:7], v[180:181] op_sel_hi:[1,0,1]
	v_mul_f32_e32 v180, s24, v188
	v_mul_f32_e32 v181, s24, v189
	v_pk_fma_f32 v[84:85], v[84:85], s[6:7], v[180:181] op_sel_hi:[1,0,1]
	v_pk_fma_f32 v[82:83], v[82:83], s[6:7], v[186:187] op_sel_hi:[1,0,1]
	s_waitcnt vmcnt(12)
	v_mul_f32_e32 v180, s24, v200
	v_mul_f32_e32 v181, s24, v201
	v_mul_f32_e32 v186, s24, v198
	v_mul_f32_e32 v187, s24, v199
	s_waitcnt vmcnt(7)
	v_mul_f32_e32 v94, s24, v94
	v_mul_f32_e32 v95, s24, v95
	v_mul_f32_e32 v96, s24, v96
	v_mul_f32_e32 v97, s24, v97
	v_pk_fma_f32 v[94:95], v[50:51], s[6:7], v[94:95] op_sel_hi:[1,0,1]
	s_waitcnt vmcnt(4)
	v_mul_f32_e32 v50, s24, v156
	v_mul_f32_e32 v51, s24, v157
	v_mul_f32_e32 v154, s24, v154
	v_mul_f32_e32 v155, s24, v155
	v_pk_fma_f32 v[96:97], v[52:53], s[6:7], v[96:97] op_sel_hi:[1,0,1]
	v_pk_fma_f32 v[52:53], v[88:89], s[6:7], v[50:51] op_sel_hi:[1,0,1]
	v_pk_fma_f32 v[50:51], v[86:87], s[6:7], v[154:155] op_sel_hi:[1,0,1]
	v_mul_f32_e32 v86, s24, v152
	v_mul_f32_e32 v87, s24, v153
	v_mul_f32_e32 v88, s24, v150
	v_mul_f32_e32 v89, s24, v151
	v_pk_fma_f32 v[56:57], v[56:57], s[6:7], v[86:87] op_sel_hi:[1,0,1]
	s_waitcnt vmcnt(2)
	v_mul_f32_e32 v86, s24, v148
	v_mul_f32_e32 v87, s24, v149
	v_pk_fma_f32 v[54:55], v[54:55], s[6:7], v[88:89] op_sel_hi:[1,0,1]
	v_mul_f32_e32 v88, s24, v146
	v_mul_f32_e32 v89, s24, v147
	v_pk_fma_f32 v[80:81], v[80:81], s[6:7], v[86:87] op_sel_hi:[1,0,1]
	v_mul_f32_e32 v86, s24, v140
	v_mul_f32_e32 v87, s24, v141
	v_mul_f32_e32 v138, s24, v138
	v_mul_f32_e32 v139, s24, v139
	v_pk_fma_f32 v[78:79], v[78:79], s[6:7], v[88:89] op_sel_hi:[1,0,1]
	v_pk_fma_f32 v[88:89], v[44:45], s[6:7], v[86:87] op_sel_hi:[1,0,1]
	v_pk_fma_f32 v[86:87], v[42:43], s[6:7], v[138:139] op_sel_hi:[1,0,1]
	s_waitcnt vmcnt(0)
	v_mul_f32_e32 v42, s24, v144
	v_mul_f32_e32 v43, s24, v145
	v_mul_f32_e32 v138, s24, v142
	v_mul_f32_e32 v139, s24, v143
	v_pk_fma_f32 v[44:45], v[132:133], s[6:7], v[42:43] op_sel_hi:[1,0,1]
	v_pk_fma_f32 v[42:43], v[130:131], s[6:7], v[138:139] op_sel_hi:[1,0,1]
	v_mul_f32_e32 v130, s24, v136
	v_mul_f32_e32 v131, s24, v137
	v_mul_f32_e32 v132, s24, v134
	v_mul_f32_e32 v133, s24, v135
	v_pk_fma_f32 v[48:49], v[48:49], s[6:7], v[130:131] op_sel_hi:[1,0,1]
	v_add_f32_e32 v130, v122, v123
	v_add_f32_e32 v131, v124, v125
	v_pk_fma_f32 v[46:47], v[46:47], s[6:7], v[132:133] op_sel_hi:[1,0,1]
	v_add_f32_e32 v130, v130, v131
	v_mul_f32_e32 v131, v123, v123
	v_mul_f32_e32 v132, v125, v125
	v_fmac_f32_e32 v131, v122, v122
	v_fmac_f32_e32 v132, v124, v124
	v_add_f32_e32 v131, v131, v132
	v_add_f32_e32 v132, v126, v127
	v_add_f32_e32 v133, v128, v129
	v_add_f32_e32 v130, 0, v130
	v_add_f32_e32 v132, v132, v133
	v_add_f32_e32 v130, v132, v130
	v_mul_f32_e32 v132, v127, v127
	v_mul_f32_e32 v133, v129, v129
	v_fmac_f32_e32 v132, v126, v126
	v_fmac_f32_e32 v133, v128, v128
	v_add_f32_e32 v132, v132, v133
	v_add_f32_e32 v131, v131, v132
	v_add_f32_e32 v132, v30, v31
	v_add_f32_e32 v133, v32, v33
	v_add_f32_e32 v132, v132, v133
	v_add_f32_e32 v130, v132, v130
	v_mul_f32_e32 v132, v31, v31
	v_mul_f32_e32 v133, v33, v33
	v_fmac_f32_e32 v132, v30, v30
	v_fmac_f32_e32 v133, v32, v32
	v_add_f32_e32 v132, v132, v133
	v_add_f32_e32 v131, v132, v131
	v_add_f32_e32 v132, v34, v35
	v_add_f32_e32 v133, v36, v37
	v_add_f32_e32 v132, v132, v133
	v_add_f32_e32 v130, v132, v130
	v_mul_f32_e32 v132, v35, v35
	v_mul_f32_e32 v133, v37, v37
	v_fmac_f32_e32 v132, v34, v34
	v_fmac_f32_e32 v133, v36, v36
	v_add_f32_e32 v132, v132, v133
	v_add_f32_e32 v132, v132, v131
	ds_swizzle_b32 v131, v130 offset:swizzle(SWAP,16)
	v_pk_fma_f32 v[28:29], v[28:29], s[6:7], v[180:181] op_sel_hi:[1,0,1]
	v_pk_fma_f32 v[26:27], v[26:27], s[6:7], v[186:187] op_sel_hi:[1,0,1]
	v_mul_f32_e32 v180, s24, v196
	v_mul_f32_e32 v181, s24, v197
	v_mul_f32_e32 v186, s24, v194
	v_mul_f32_e32 v187, s24, v195
	v_pk_fma_f32 v[40:41], v[40:41], s[6:7], v[180:181] op_sel_hi:[1,0,1]
	v_pk_fma_f32 v[38:39], v[38:39], s[6:7], v[186:187] op_sel_hi:[1,0,1]
	v_mul_f32_e32 v180, s24, v210
	v_mul_f32_e32 v181, s24, v211
	v_mul_f32_e32 v186, s24, v208
	v_mul_f32_e32 v187, s24, v209
	s_waitcnt lgkmcnt(0)
	v_add_f32_e32 v131, v130, v131
	ds_swizzle_b32 v130, v132 offset:swizzle(SWAP,16)
	v_pk_fma_f32 v[68:69], v[68:69], s[6:7], v[180:181] op_sel_hi:[1,0,1]
	v_pk_fma_f32 v[66:67], v[66:67], s[6:7], v[186:187] op_sel_hi:[1,0,1]
	v_mul_f32_e32 v180, s24, v206
	v_mul_f32_e32 v181, s24, v207
	v_mul_f32_e32 v186, s24, v204
	v_mul_f32_e32 v187, s24, v205
	v_pk_fma_f32 v[72:73], v[72:73], s[6:7], v[180:181] op_sel_hi:[1,0,1]
	v_pk_fma_f32 v[70:71], v[70:71], s[6:7], v[186:187] op_sel_hi:[1,0,1]
	v_mul_f32_e32 v180, s24, v218
	v_mul_f32_e32 v181, s24, v219
	v_mul_f32_e32 v186, s24, v216
	v_mul_f32_e32 v187, s24, v217
	v_mul_f32_e32 v190, s24, v190
	v_mul_f32_e32 v191, s24, v191
	v_pk_fma_f32 v[60:61], v[60:61], s[6:7], v[180:181] op_sel_hi:[1,0,1]
	v_pk_fma_f32 v[58:59], v[58:59], s[6:7], v[186:187] op_sel_hi:[1,0,1]
	v_mul_f32_e32 v180, s24, v214
	v_mul_f32_e32 v181, s24, v215
	v_mul_f32_e32 v186, s24, v212
	v_mul_f32_e32 v187, s24, v213
	v_mul_f32_e32 v160, s24, v160
	v_mul_f32_e32 v161, s24, v161
	v_mul_f32_e32 v158, s24, v158
	v_mul_f32_e32 v159, s24, v159
	v_pk_fma_f32 v[74:75], v[74:75], s[6:7], v[190:191] op_sel_hi:[1,0,1]
	v_pk_fma_f32 v[64:65], v[64:65], s[6:7], v[180:181] op_sel_hi:[1,0,1]
	v_pk_fma_f32 v[62:63], v[62:63], s[6:7], v[186:187] op_sel_hi:[1,0,1]
	v_pk_fma_f32 v[92:93], v[92:93], s[6:7], v[160:161] op_sel_hi:[1,0,1]
	v_pk_fma_f32 v[90:91], v[90:91], s[6:7], v[158:159] op_sel_hi:[1,0,1]
	s_waitcnt lgkmcnt(0)
	v_add_f32_e32 v130, v132, v130
	v_mov_b32_e32 v133, v131
	v_mov_b32_e32 v132, v130
	s_nop 0
	v_permlane32_swap_b32_e32 v131, v133
	v_permlane32_swap_b32_e32 v130, v132
	s_and_saveexec_b64 s[6:7], vcc
	s_mov_b64 s[52:53], 0x400
	s_mov_b32 s36, s17
	s_cbranch_execz .LBB0_580
	v_pk_add_f32 v[130:131], v[130:131], v[132:133]
	s_lshl_b32 s9, s8, 11
	v_mul_f32_e32 v132, 0x3c800000, v131
	v_fma_f32 v130, -v131, v132, v130
	s_add_i32 s9, s5, s9
	v_max_f32_e32 v133, 0, v130
	v_lshl_add_u32 v130, v0, 5, s9
	ds_write_b64 v130, v[132:133]

.LBB0_1803:
	v_and_b32_e32 v231, 63, v130
	v_bfe_u32 v232, v130, 4, 2
	s_lshl_b32 s1, s29, 5
	s_lshl_b32 s0, s31, 8
	s_barrier
	s_or_b32 s1, s0, s1
	v_add_u32_e32 v230, s44, v0
	v_lshl_add_u32 v194, v232, 3, s1
	v_lshl_add_u32 v228, s18, 8, v230
	v_ashrrev_i32_e32 v195, 31, v194
	v_ashrrev_i32_e32 v229, 31, v228
	v_lshl_add_u64 v[142:143], v[194:195], 1, s[12:13]
	v_lshlrev_b64 v[130:131], 12, v[228:229]
	s_mov_b32 s2, 1.0
	s_mov_b32 s20, 0x3fd744fd
	v_lshl_add_u64 v[226:227], v[142:143], 0, v[130:131]
	global_load_dwordx4 v[190:193], v[226:227], off
	global_load_dwordx4 v[186:189], v[226:227], off offset:256
	v_add_u32_e32 v224, 16, v228
	v_ashrrev_i32_e32 v225, 31, v224
	v_lshlrev_b64 v[130:131], 12, v[224:225]
	v_lshl_add_u64 v[222:223], v[142:143], 0, v[130:131]
	global_load_dwordx4 v[182:185], v[222:223], off
	global_load_dwordx4 v[178:181], v[222:223], off offset:256
	v_add_u32_e32 v220, 32, v228
	v_ashrrev_i32_e32 v221, 31, v220
	v_lshlrev_b64 v[130:131], 12, v[220:221]
	v_lshl_add_u64 v[218:219], v[142:143], 0, v[130:131]
	global_load_dwordx4 v[174:177], v[218:219], off
	global_load_dwordx4 v[170:173], v[218:219], off offset:256
	v_add_u32_e32 v216, 48, v228
	v_ashrrev_i32_e32 v217, 31, v216
	v_lshlrev_b64 v[130:131], 12, v[216:217]
	v_lshl_add_u64 v[214:215], v[142:143], 0, v[130:131]
	global_load_dwordx4 v[166:169], v[214:215], off
	global_load_dwordx4 v[162:165], v[214:215], off offset:256
	v_add_u32_e32 v212, 0x80, v228
	v_ashrrev_i32_e32 v213, 31, v212
	v_lshlrev_b64 v[130:131], 12, v[212:213]
	v_lshl_add_u64 v[210:211], v[142:143], 0, v[130:131]
	global_load_dwordx4 v[158:161], v[210:211], off
	global_load_dwordx4 v[154:157], v[210:211], off offset:256
	v_add_u32_e32 v208, 0x90, v228
	v_ashrrev_i32_e32 v209, 31, v208
	v_lshlrev_b64 v[130:131], 12, v[208:209]
	v_lshl_add_u64 v[206:207], v[142:143], 0, v[130:131]
	global_load_dwordx4 v[146:149], v[206:207], off
	global_load_dwordx4 v[138:141], v[206:207], off offset:256
	v_add_u32_e32 v204, 0xa0, v228
	v_ashrrev_i32_e32 v205, 31, v204
	v_lshlrev_b64 v[130:131], 12, v[204:205]
	v_lshl_add_u64 v[200:201], v[142:143], 0, v[130:131]
	global_load_dwordx4 v[134:137], v[200:201], off
	global_load_dwordx4 v[130:133], v[200:201], off offset:256
	v_add_u32_e32 v196, 0xb0, v228
	v_ashrrev_i32_e32 v197, 31, v196
	v_lshlrev_b64 v[144:145], 12, v[196:197]
	v_lshl_add_u64 v[198:199], v[142:143], 0, v[144:145]
	global_load_dwordx4 v[150:153], v[198:199], off
	global_load_dwordx4 v[142:145], v[198:199], off offset:256
	s_lshl_b32 s1, s29, 3
	v_cmp_eq_u32_e32 vcc, 0, v232
	s_add_i32 s1, s1, 0
	s_waitcnt vmcnt(15)
	v_lshlrev_b32_e32 v238, 16, v192
	v_and_b32_e32 v239, 0xffff0000, v192
	v_lshlrev_b32_e32 v192, 16, v193
	v_and_b32_e32 v193, 0xffff0000, v193
	v_lshlrev_b32_e32 v240, 16, v190
	v_and_b32_e32 v241, 0xffff0000, v190
	v_lshlrev_b32_e32 v190, 16, v191
	v_and_b32_e32 v191, 0xffff0000, v191
	v_mul_f32_e32 v190, s20, v190
	v_mul_f32_e32 v191, s20, v191
	v_mul_f32_e32 v192, s20, v192
	v_mul_f32_e32 v193, s20, v193
	v_pk_fma_f32 v[124:125], v[124:125], s[2:3], v[190:191] op_sel_hi:[1,0,1]
	v_mul_f32_e32 v190, s20, v238
	v_mul_f32_e32 v191, s20, v239
	v_pk_fma_f32 v[128:129], v[128:129], s[2:3], v[192:193] op_sel_hi:[1,0,1]
	s_waitcnt vmcnt(14)
	v_lshlrev_b32_e32 v192, 16, v186
	v_and_b32_e32 v193, 0xffff0000, v186
	v_lshlrev_b32_e32 v186, 16, v187
	v_and_b32_e32 v187, 0xffff0000, v187
	v_pk_fma_f32 v[126:127], v[126:127], s[2:3], v[190:191] op_sel_hi:[1,0,1]
	v_lshlrev_b32_e32 v190, 16, v188
	v_and_b32_e32 v191, 0xffff0000, v188
	v_lshlrev_b32_e32 v188, 16, v189
	v_and_b32_e32 v189, 0xffff0000, v189
	v_mul_f32_e32 v186, s20, v186
	v_mul_f32_e32 v187, s20, v187
	v_pk_fma_f32 v[60:61], v[60:61], s[2:3], v[186:187] op_sel_hi:[1,0,1]
	v_mul_f32_e32 v186, s20, v190
	v_mul_f32_e32 v187, s20, v191
	v_mul_f32_e32 v188, s20, v188
	v_mul_f32_e32 v189, s20, v189
	v_pk_fma_f32 v[64:65], v[64:65], s[2:3], v[188:189] op_sel_hi:[1,0,1]
	v_pk_fma_f32 v[62:63], v[62:63], s[2:3], v[186:187] op_sel_hi:[1,0,1]
	s_waitcnt vmcnt(13)
	v_lshlrev_b32_e32 v186, 16, v184
	v_and_b32_e32 v187, 0xffff0000, v184
	v_lshlrev_b32_e32 v184, 16, v185
	v_and_b32_e32 v185, 0xffff0000, v185
	v_lshlrev_b32_e32 v188, 16, v182
	v_and_b32_e32 v189, 0xffff0000, v182
	v_lshlrev_b32_e32 v182, 16, v183
	v_and_b32_e32 v183, 0xffff0000, v183
	v_mul_f32_e32 v182, s20, v182
	v_mul_f32_e32 v183, s20, v183
	v_mul_f32_e32 v184, s20, v184
	v_mul_f32_e32 v185, s20, v185
	v_pk_fma_f32 v[116:117], v[116:117], s[2:3], v[182:183] op_sel_hi:[1,0,1]
	v_mul_f32_e32 v182, s20, v186
	v_mul_f32_e32 v183, s20, v187
	v_pk_fma_f32 v[120:121], v[120:121], s[2:3], v[184:185] op_sel_hi:[1,0,1]
	s_waitcnt vmcnt(12)
	v_lshlrev_b32_e32 v184, 16, v178
	v_and_b32_e32 v185, 0xffff0000, v178
	v_lshlrev_b32_e32 v178, 16, v179
	v_and_b32_e32 v179, 0xffff0000, v179
	v_pk_fma_f32 v[118:119], v[118:119], s[2:3], v[182:183] op_sel_hi:[1,0,1]
	v_lshlrev_b32_e32 v182, 16, v180
	v_and_b32_e32 v183, 0xffff0000, v180
	v_lshlrev_b32_e32 v180, 16, v181
	v_and_b32_e32 v181, 0xffff0000, v181
	v_mul_f32_e32 v178, s20, v178
	v_mul_f32_e32 v179, s20, v179
	v_pk_fma_f32 v[52:53], v[52:53], s[2:3], v[178:179] op_sel_hi:[1,0,1]
	v_mul_f32_e32 v178, s20, v182
	v_mul_f32_e32 v179, s20, v183
	v_mul_f32_e32 v180, s20, v180
	v_mul_f32_e32 v181, s20, v181
	v_pk_fma_f32 v[56:57], v[56:57], s[2:3], v[180:181] op_sel_hi:[1,0,1]
	v_pk_fma_f32 v[54:55], v[54:55], s[2:3], v[178:179] op_sel_hi:[1,0,1]
	s_waitcnt vmcnt(11)
	v_lshlrev_b32_e32 v178, 16, v176
	v_and_b32_e32 v179, 0xffff0000, v176
	v_lshlrev_b32_e32 v176, 16, v177
	v_and_b32_e32 v177, 0xffff0000, v177
	v_lshlrev_b32_e32 v180, 16, v174
	v_and_b32_e32 v181, 0xffff0000, v174
	v_lshlrev_b32_e32 v174, 16, v175
	v_and_b32_e32 v175, 0xffff0000, v175
	v_mul_f32_e32 v174, s20, v174
	v_mul_f32_e32 v175, s20, v175
	v_mul_f32_e32 v176, s20, v176
	v_mul_f32_e32 v177, s20, v177
	v_pk_fma_f32 v[112:113], v[112:113], s[2:3], v[174:175] op_sel_hi:[1,0,1]
	v_mul_f32_e32 v174, s20, v178
	v_mul_f32_e32 v175, s20, v179
	v_pk_fma_f32 v[108:109], v[108:109], s[2:3], v[176:177] op_sel_hi:[1,0,1]
	s_waitcnt vmcnt(10)
	v_lshlrev_b32_e32 v176, 16, v170
	v_and_b32_e32 v177, 0xffff0000, v170
	v_lshlrev_b32_e32 v170, 16, v171
	v_and_b32_e32 v171, 0xffff0000, v171
	v_pk_fma_f32 v[106:107], v[106:107], s[2:3], v[174:175] op_sel_hi:[1,0,1]
	v_lshlrev_b32_e32 v174, 16, v172
	v_and_b32_e32 v175, 0xffff0000, v172
	v_lshlrev_b32_e32 v172, 16, v173
	v_and_b32_e32 v173, 0xffff0000, v173
	v_mul_f32_e32 v170, s20, v170
	v_mul_f32_e32 v171, s20, v171
	v_pk_fma_f32 v[44:45], v[44:45], s[2:3], v[170:171] op_sel_hi:[1,0,1]
	v_mul_f32_e32 v170, s20, v174
	v_mul_f32_e32 v171, s20, v175
	v_mul_f32_e32 v172, s20, v172
	v_mul_f32_e32 v173, s20, v173
	v_pk_fma_f32 v[48:49], v[48:49], s[2:3], v[172:173] op_sel_hi:[1,0,1]
	v_pk_fma_f32 v[46:47], v[46:47], s[2:3], v[170:171] op_sel_hi:[1,0,1]
	s_waitcnt vmcnt(9)
	v_lshlrev_b32_e32 v170, 16, v168
	v_and_b32_e32 v171, 0xffff0000, v168
	v_lshlrev_b32_e32 v168, 16, v169
	v_and_b32_e32 v169, 0xffff0000, v169
	v_lshlrev_b32_e32 v172, 16, v166
	v_and_b32_e32 v173, 0xffff0000, v166
	v_lshlrev_b32_e32 v166, 16, v167
	v_and_b32_e32 v167, 0xffff0000, v167
	v_mul_f32_e32 v166, s20, v166
	v_mul_f32_e32 v167, s20, v167
	v_mul_f32_e32 v168, s20, v168
	v_mul_f32_e32 v169, s20, v169
	v_pk_fma_f32 v[100:101], v[100:101], s[2:3], v[166:167] op_sel_hi:[1,0,1]
	v_mul_f32_e32 v166, s20, v170
	v_mul_f32_e32 v167, s20, v171
	v_pk_fma_f32 v[104:105], v[104:105], s[2:3], v[168:169] op_sel_hi:[1,0,1]
	s_waitcnt vmcnt(8)
	v_lshlrev_b32_e32 v168, 16, v162
	v_and_b32_e32 v169, 0xffff0000, v162
	v_lshlrev_b32_e32 v162, 16, v163
	v_and_b32_e32 v163, 0xffff0000, v163
	v_pk_fma_f32 v[102:103], v[102:103], s[2:3], v[166:167] op_sel_hi:[1,0,1]
	v_lshlrev_b32_e32 v166, 16, v164
	v_and_b32_e32 v167, 0xffff0000, v164
	v_lshlrev_b32_e32 v164, 16, v165
	v_and_b32_e32 v165, 0xffff0000, v165
	v_mul_f32_e32 v162, s20, v162
	v_mul_f32_e32 v163, s20, v163
	v_pk_fma_f32 v[36:37], v[36:37], s[2:3], v[162:163] op_sel_hi:[1,0,1]
	v_mul_f32_e32 v162, s20, v166
	v_mul_f32_e32 v163, s20, v167
	v_mul_f32_e32 v164, s20, v164
	v_mul_f32_e32 v165, s20, v165
	v_pk_fma_f32 v[40:41], v[40:41], s[2:3], v[164:165] op_sel_hi:[1,0,1]
	v_pk_fma_f32 v[38:39], v[38:39], s[2:3], v[162:163] op_sel_hi:[1,0,1]
	s_waitcnt vmcnt(7)
	v_lshlrev_b32_e32 v162, 16, v160
	v_and_b32_e32 v163, 0xffff0000, v160
	v_lshlrev_b32_e32 v160, 16, v161
	v_and_b32_e32 v161, 0xffff0000, v161
	v_lshlrev_b32_e32 v164, 16, v158
	v_and_b32_e32 v165, 0xffff0000, v158
	v_lshlrev_b32_e32 v158, 16, v159
	v_and_b32_e32 v159, 0xffff0000, v159
	v_mul_f32_e32 v158, s20, v158
	v_mul_f32_e32 v159, s20, v159
	v_mul_f32_e32 v160, s20, v160
	v_mul_f32_e32 v161, s20, v161
	v_pk_fma_f32 v[92:93], v[92:93], s[2:3], v[158:159] op_sel_hi:[1,0,1]
	v_mul_f32_e32 v158, s20, v162
	v_mul_f32_e32 v159, s20, v163
	v_pk_fma_f32 v[96:97], v[96:97], s[2:3], v[160:161] op_sel_hi:[1,0,1]
	s_waitcnt vmcnt(6)
	v_lshlrev_b32_e32 v160, 16, v154
	v_and_b32_e32 v161, 0xffff0000, v154
	v_lshlrev_b32_e32 v154, 16, v155
	v_and_b32_e32 v155, 0xffff0000, v155
	v_pk_fma_f32 v[94:95], v[94:95], s[2:3], v[158:159] op_sel_hi:[1,0,1]
	v_lshlrev_b32_e32 v158, 16, v156
	v_and_b32_e32 v159, 0xffff0000, v156
	v_lshlrev_b32_e32 v156, 16, v157
	v_and_b32_e32 v157, 0xffff0000, v157
	v_mul_f32_e32 v154, s20, v154
	v_mul_f32_e32 v155, s20, v155
	v_pk_fma_f32 v[28:29], v[28:29], s[2:3], v[154:155] op_sel_hi:[1,0,1]
	v_mul_f32_e32 v154, s20, v158
	v_mul_f32_e32 v155, s20, v159
	v_mul_f32_e32 v156, s20, v156
	v_mul_f32_e32 v157, s20, v157
	v_pk_fma_f32 v[32:33], v[32:33], s[2:3], v[156:157] op_sel_hi:[1,0,1]
	v_pk_fma_f32 v[30:31], v[30:31], s[2:3], v[154:155] op_sel_hi:[1,0,1]
	s_waitcnt vmcnt(5)
	v_lshlrev_b32_e32 v154, 16, v148
	v_and_b32_e32 v155, 0xffff0000, v148
	v_lshlrev_b32_e32 v148, 16, v149
	v_and_b32_e32 v149, 0xffff0000, v149
	v_lshlrev_b32_e32 v156, 16, v146
	v_and_b32_e32 v157, 0xffff0000, v146
	v_lshlrev_b32_e32 v146, 16, v147
	v_and_b32_e32 v147, 0xffff0000, v147
	v_mul_f32_e32 v146, s20, v146
	v_mul_f32_e32 v147, s20, v147
	v_mul_f32_e32 v148, s20, v148
	v_mul_f32_e32 v149, s20, v149
	v_pk_fma_f32 v[84:85], v[84:85], s[2:3], v[146:147] op_sel_hi:[1,0,1]
	v_mul_f32_e32 v146, s20, v154
	v_mul_f32_e32 v147, s20, v155
	v_pk_fma_f32 v[88:89], v[88:89], s[2:3], v[148:149] op_sel_hi:[1,0,1]
	s_waitcnt vmcnt(4)
	v_lshlrev_b32_e32 v148, 16, v138
	v_and_b32_e32 v149, 0xffff0000, v138
	v_lshlrev_b32_e32 v138, 16, v139
	v_and_b32_e32 v139, 0xffff0000, v139
	v_pk_fma_f32 v[86:87], v[86:87], s[2:3], v[146:147] op_sel_hi:[1,0,1]
	v_lshlrev_b32_e32 v146, 16, v140
	v_and_b32_e32 v147, 0xffff0000, v140
	v_lshlrev_b32_e32 v140, 16, v141
	v_and_b32_e32 v141, 0xffff0000, v141
	v_mul_f32_e32 v138, s20, v138
	v_mul_f32_e32 v139, s20, v139
	v_pk_fma_f32 v[20:21], v[20:21], s[2:3], v[138:139] op_sel_hi:[1,0,1]
	v_mul_f32_e32 v138, s20, v146
	v_mul_f32_e32 v139, s20, v147
	v_mul_f32_e32 v140, s20, v140
	v_mul_f32_e32 v141, s20, v141
	v_pk_fma_f32 v[24:25], v[24:25], s[2:3], v[140:141] op_sel_hi:[1,0,1]
	v_pk_fma_f32 v[22:23], v[22:23], s[2:3], v[138:139] op_sel_hi:[1,0,1]
	s_waitcnt vmcnt(3)
	v_lshlrev_b32_e32 v138, 16, v136
	v_and_b32_e32 v139, 0xffff0000, v136
	v_lshlrev_b32_e32 v136, 16, v137
	v_and_b32_e32 v137, 0xffff0000, v137
	v_lshlrev_b32_e32 v140, 16, v134
	v_and_b32_e32 v141, 0xffff0000, v134
	v_lshlrev_b32_e32 v134, 16, v135
	v_and_b32_e32 v135, 0xffff0000, v135
	v_mul_f32_e32 v134, s20, v134
	v_mul_f32_e32 v135, s20, v135
	v_mul_f32_e32 v136, s20, v136
	v_mul_f32_e32 v137, s20, v137
	v_pk_fma_f32 v[76:77], v[76:77], s[2:3], v[134:135] op_sel_hi:[1,0,1]
	v_mul_f32_e32 v134, s20, v138
	v_mul_f32_e32 v135, s20, v139
	v_pk_fma_f32 v[80:81], v[80:81], s[2:3], v[136:137] op_sel_hi:[1,0,1]
	s_waitcnt vmcnt(2)
	v_lshlrev_b32_e32 v136, 16, v130
	v_and_b32_e32 v137, 0xffff0000, v130
	v_lshlrev_b32_e32 v130, 16, v131
	v_and_b32_e32 v131, 0xffff0000, v131
	v_pk_fma_f32 v[78:79], v[78:79], s[2:3], v[134:135] op_sel_hi:[1,0,1]
	v_lshlrev_b32_e32 v134, 16, v132
	v_and_b32_e32 v135, 0xffff0000, v132
	v_mul_f32_e32 v130, s20, v130
	v_mul_f32_e32 v131, s20, v131
	v_lshlrev_b32_e32 v132, 16, v133
	v_and_b32_e32 v133, 0xffff0000, v133
	v_pk_fma_f32 v[12:13], v[12:13], s[2:3], v[130:131] op_sel_hi:[1,0,1]
	v_mul_f32_e32 v130, s20, v134
	v_mul_f32_e32 v131, s20, v135
	v_mul_f32_e32 v132, s20, v132
	v_mul_f32_e32 v133, s20, v133
	v_pk_fma_f32 v[14:15], v[14:15], s[2:3], v[130:131] op_sel_hi:[1,0,1]
	s_waitcnt vmcnt(1)
	v_lshlrev_b32_e32 v130, 16, v152
	v_and_b32_e32 v131, 0xffff0000, v152
	v_pk_fma_f32 v[16:17], v[16:17], s[2:3], v[132:133] op_sel_hi:[1,0,1]
	v_lshlrev_b32_e32 v132, 16, v153
	v_and_b32_e32 v133, 0xffff0000, v153
	v_mul_f32_e32 v130, s20, v130
	v_mul_f32_e32 v131, s20, v131
	v_mul_f32_e32 v240, s20, v240
	v_mul_f32_e32 v241, s20, v241
	v_mul_f32_e32 v192, s20, v192
	v_mul_f32_e32 v193, s20, v193
	v_mul_f32_e32 v132, s20, v132
	v_mul_f32_e32 v133, s20, v133
	v_pk_fma_f32 v[70:71], v[70:71], s[2:3], v[130:131] op_sel_hi:[1,0,1]
	s_waitcnt vmcnt(0)
	v_lshlrev_b32_e32 v130, 16, v144
	v_and_b32_e32 v131, 0xffff0000, v144
	v_pk_fma_f32 v[122:123], v[122:123], s[2:3], v[240:241] op_sel_hi:[1,0,1]
	v_pk_fma_f32 v[58:59], v[58:59], s[2:3], v[192:193] op_sel_hi:[1,0,1]
	v_pk_fma_f32 v[72:73], v[72:73], s[2:3], v[132:133] op_sel_hi:[1,0,1]
	v_lshlrev_b32_e32 v132, 16, v145
	v_and_b32_e32 v133, 0xffff0000, v145
	v_mul_f32_e32 v130, s20, v130
	v_mul_f32_e32 v131, s20, v131
	v_mul_f32_e32 v132, s20, v132
	v_mul_f32_e32 v133, s20, v133
	v_pk_fma_f32 v[6:7], v[6:7], s[2:3], v[130:131] op_sel_hi:[1,0,1]
	v_add_f32_e32 v130, v122, v123
	v_add_f32_e32 v131, v124, v125
	v_pk_fma_f32 v[8:9], v[8:9], s[2:3], v[132:133] op_sel_hi:[1,0,1]
	v_add_f32_e32 v130, v130, v131
	v_mul_f32_e32 v131, v123, v123
	v_mul_f32_e32 v132, v125, v125
	v_fmac_f32_e32 v131, v122, v122
	v_fmac_f32_e32 v132, v124, v124
	v_add_f32_e32 v131, v131, v132
	v_add_f32_e32 v132, v126, v127
	v_add_f32_e32 v133, v128, v129
	v_add_f32_e32 v130, 0, v130
	v_add_f32_e32 v132, v132, v133
	v_add_f32_e32 v130, v132, v130
	v_mul_f32_e32 v132, v127, v127
	v_mul_f32_e32 v133, v129, v129
	v_fmac_f32_e32 v132, v126, v126
	v_fmac_f32_e32 v133, v128, v128
	v_add_f32_e32 v132, v132, v133
	v_add_f32_e32 v131, v131, v132
	v_add_f32_e32 v132, v58, v59
	v_add_f32_e32 v133, v60, v61
	v_add_f32_e32 v132, v132, v133
	v_add_f32_e32 v130, v132, v130
	v_mul_f32_e32 v132, v59, v59
	v_mul_f32_e32 v133, v61, v61
	v_fmac_f32_e32 v132, v58, v58
	v_fmac_f32_e32 v133, v60, v60
	v_add_f32_e32 v132, v132, v133
	v_add_f32_e32 v131, v132, v131
	v_add_f32_e32 v132, v62, v63
	v_add_f32_e32 v133, v64, v65
	v_add_f32_e32 v132, v132, v133
	v_add_f32_e32 v130, v132, v130
	v_mul_f32_e32 v132, v63, v63
	v_mul_f32_e32 v133, v65, v65
	v_fmac_f32_e32 v132, v62, v62
	v_fmac_f32_e32 v133, v64, v64
	v_add_f32_e32 v132, v132, v133
	v_add_f32_e32 v132, v132, v131
	ds_swizzle_b32 v131, v130 offset:swizzle(SWAP,16)
	v_mul_f32_e32 v136, s20, v136
	v_mul_f32_e32 v137, s20, v137
	v_pk_fma_f32 v[10:11], v[10:11], s[2:3], v[136:137] op_sel_hi:[1,0,1]
	v_lshlrev_b32_e32 v134, 16, v150
	v_and_b32_e32 v135, 0xffff0000, v150
	v_lshlrev_b32_e32 v136, 16, v151
	v_and_b32_e32 v137, 0xffff0000, v151
	s_waitcnt lgkmcnt(0)
	v_add_f32_e32 v131, v130, v131
	ds_swizzle_b32 v130, v132 offset:swizzle(SWAP,16)
	v_mul_f32_e32 v134, s20, v134
	v_mul_f32_e32 v135, s20, v135
	v_mul_f32_e32 v136, s20, v136
	v_mul_f32_e32 v137, s20, v137
	v_pk_fma_f32 v[68:69], v[68:69], s[2:3], v[136:137] op_sel_hi:[1,0,1]
	v_pk_fma_f32 v[66:67], v[66:67], s[2:3], v[134:135] op_sel_hi:[1,0,1]
	v_lshlrev_b32_e32 v134, 16, v142
	v_and_b32_e32 v135, 0xffff0000, v142
	v_lshlrev_b32_e32 v136, 16, v143
	v_and_b32_e32 v137, 0xffff0000, v143
	v_mul_f32_e32 v188, s20, v188
	v_mul_f32_e32 v189, s20, v189
	v_mul_f32_e32 v184, s20, v184
	v_mul_f32_e32 v185, s20, v185
	v_mul_f32_e32 v180, s20, v180
	v_mul_f32_e32 v181, s20, v181
	v_mul_f32_e32 v176, s20, v176
	v_mul_f32_e32 v177, s20, v177
	v_mul_f32_e32 v172, s20, v172
	v_mul_f32_e32 v173, s20, v173
	v_mul_f32_e32 v168, s20, v168
	v_mul_f32_e32 v169, s20, v169
	v_mul_f32_e32 v164, s20, v164
	v_mul_f32_e32 v165, s20, v165
	v_mul_f32_e32 v160, s20, v160
	v_mul_f32_e32 v161, s20, v161
	v_mul_f32_e32 v156, s20, v156
	v_mul_f32_e32 v157, s20, v157
	v_mul_f32_e32 v148, s20, v148
	v_mul_f32_e32 v149, s20, v149
	v_mul_f32_e32 v140, s20, v140
	v_mul_f32_e32 v141, s20, v141
	v_mul_f32_e32 v134, s20, v134
	v_mul_f32_e32 v135, s20, v135
	v_mul_f32_e32 v136, s20, v136
	v_mul_f32_e32 v137, s20, v137
	v_pk_fma_f32 v[114:115], v[114:115], s[2:3], v[188:189] op_sel_hi:[1,0,1]
	v_pk_fma_f32 v[50:51], v[50:51], s[2:3], v[184:185] op_sel_hi:[1,0,1]
	v_pk_fma_f32 v[110:111], v[110:111], s[2:3], v[180:181] op_sel_hi:[1,0,1]
	v_pk_fma_f32 v[42:43], v[42:43], s[2:3], v[176:177] op_sel_hi:[1,0,1]
	v_pk_fma_f32 v[98:99], v[98:99], s[2:3], v[172:173] op_sel_hi:[1,0,1]
	v_pk_fma_f32 v[34:35], v[34:35], s[2:3], v[168:169] op_sel_hi:[1,0,1]
	v_pk_fma_f32 v[90:91], v[90:91], s[2:3], v[164:165] op_sel_hi:[1,0,1]
	v_pk_fma_f32 v[26:27], v[26:27], s[2:3], v[160:161] op_sel_hi:[1,0,1]
	v_pk_fma_f32 v[82:83], v[82:83], s[2:3], v[156:157] op_sel_hi:[1,0,1]
	v_pk_fma_f32 v[18:19], v[18:19], s[2:3], v[148:149] op_sel_hi:[1,0,1]
	v_pk_fma_f32 v[74:75], v[74:75], s[2:3], v[140:141] op_sel_hi:[1,0,1]
	v_pk_fma_f32 v[4:5], v[4:5], s[2:3], v[136:137] op_sel_hi:[1,0,1]
	v_pk_fma_f32 v[2:3], v[2:3], s[2:3], v[134:135] op_sel_hi:[1,0,1]
	s_nop 0
	s_waitcnt lgkmcnt(0)
	v_add_f32_e32 v130, v132, v130
	v_mov_b32_e32 v133, v131
	v_mov_b32_e32 v132, v130
	s_nop 0
	v_permlane32_swap_b32_e32 v131, v133
	v_permlane32_swap_b32_e32 v130, v132
	s_and_saveexec_b64 s[2:3], vcc
	s_mov_b64 s[52:53], 0x400
	s_cbranch_execz .LBB0_1805
	v_pk_add_f32 v[130:131], v[130:131], v[132:133]
	s_lshl_b32 s20, s28, 11
	v_mul_f32_e32 v132, 0x3c800000, v131
	v_fma_f32 v130, -v131, v132, v130
	s_add_i32 s20, s1, s20
	v_max_f32_e32 v133, 0, v130
	v_lshl_add_u32 v130, v0, 5, s20
	ds_write_b64 v130, v[132:133]
